# P1 K loop: first iteration of each unit no longer waits (vmcnt) on the previous unit's epilogue stores; prologue drains before the first unit
# speedup vs baseline: 1.0001x; 1.0001x over previous
; #define PG8_STAGE(bufoff, gbase, voff) do { _Pragma("unroll") for (int _i = 0; _i < 2; ++_i) \
;         __builtin_amdgcn_global_load_lds((const unsigned*)((const char*)(gbase) + (voff)[_i]), (PG8_LAS unsigned*)(lds + (bufoff) + ldsw + _i * 8192), 16, 0, 0); } while (0)
; #define PG8_WAIT_V(n) asm volatile("s_waitcnt vmcnt(" #n ")" ::: "memory")
; #define PG8_BAR __builtin_amdgcn_s_barrier()
; template <class Epi, class Sched, bool ALIGN_EPI = false, bool SP2 = false>
; __device__ __forceinline__ void gemm_phase(PG8_LAS unsigned char* lds, const Gemm g, const Sched& S, const Epi& E) {
;     ...
;     const int tid = tid_l, wid = __builtin_amdgcn_readfirstlane(tid >> 6), lane = tid & 63, wr = wid >> 2, wc = wid & 3, fr = lane & 15, fq = lane >> 4;
;     const int K = g.K, nt = K / BK;
;     unsigned voffA[2], voffB[2];
; #pragma unroll
;     for (int i = 0; i < 2; ++i) { int R, C; stage_rc(tid * 16 + i * 8192, R, C); const int Rb = Epi::PERM ? ((R & ~31) + perm32(R & 31)) : R;
;         voffA[i] = (unsigned)(R * K + C) * 2u; voffB[i] = (unsigned)(Rb * K + C) * 2u; }
;     const size_t kstep = (size_t)(BK * 2);
;     const size_t hstep = (size_t)HALF * K * 2;
;     const size_t tstep = 2 * hstep;
;     const unsigned ldsw = (unsigned)wid * 1024u;
;     const int aoff = lds_byte(wr * 64 + fr, fq * 8), boff = lds_byte(wc * 32 + fr, fq * 8);
;     ...
;         PG8_STAGE(PG8_SB(0, 0), cB, voffB); PG8_STAGE(PG8_SB(0, 1), cB + hstep, voffB); PG8_STAGE(PG8_SA(0, 0), cA, voffA); PG8_STAGE(PG8_SA(0, 1), cA + hstep, voffA);
;         if (wr == 1) PG8_BAR;
;         PG8_WAIT_V(2); PG8_BAR;
;         PG8_STAGE(PG8_SB(1, 0), cB + kstep, voffB); PG8_STAGE(PG8_SA(1, 0), cA + kstep, voffA); PG8_STAGE(PG8_SB(1, 1), cB + hstep + kstep, voffB);
;         PG8_WAIT_V(6); PG8_BAR;
.LBB0_147:
	v_readlane_b32 s4, v253, 34
	v_readlane_b32 s5, v253, 35
	s_and_b64 s[4:5], s[4:5], exec
	s_mov_b32 s4, 0x3b100000
	s_cselect_b32 s4, s4, 0x80000
	s_add_u32 s20, s10, 0x3c120000
	s_addc_u32 s21, s11, 0
	s_add_u32 s22, s10, s4
	s_addc_u32 s23, s11, 0
	s_add_u32 s63, s10, 0x63160000
	s_addc_u32 s64, s11, 0
	s_add_u32 s24, s10, 0x6f560000
	s_addc_u32 s25, s11, 0
	s_lshl_b64 s[4:5], s[16:17], 2
	s_add_u32 s4, s10, s4
	s_addc_u32 s5, s11, s5
	s_add_u32 s4, s4, 0x3400
	s_addc_u32 s5, s5, 0
	v_writelane_b32 v253, s4, 48
	s_and_b32 s28, s2, 3
	s_add_i32 m0, s59, 0x18000
	v_writelane_b32 v253, s5, 49
	v_lshl_add_u64 v[10:11], v[10:11], 0, s[78:79]
	v_readlane_b32 s4, v253, 41
	s_lshl_b32 s2, s0, 13
	s_lshl_b32 s30, s28, 5
	s_lshl_b32 s6, s28, 12
	s_add_i32 s65, s4, 1
	s_waitcnt vmcnt(2)
	s_barrier
	global_load_lds_dwordx4 v[10:11], off
	v_lshl_add_u64 v[8:9], v[8:9], 0, s[78:79]
	s_add_i32 m0, s59, 0x1a000
	s_add_i32 s66, s59, 0x8000
	s_add_i32 s67, s59, 0xa000
	v_readlane_b32 s5, v253, 42
	global_load_lds_dwordx4 v[8:9], off
	v_lshl_add_u64 v[4:5], v[4:5], 0, s[78:79]
	s_mov_b32 m0, s66
	s_add_u32 s4, s46, 0x100080
	global_load_lds_dwordx4 v[4:5], off
	v_lshl_add_u64 v[4:5], v[6:7], 0, s[78:79]
	s_mov_b32 m0, s67
	s_addc_u32 s5, s47, 0
	global_load_lds_dwordx4 v[4:5], off
	s_add_i32 m0, s59, 0x1c000
	v_lshl_add_u64 v[4:5], s[4:5], 0, v[2:3]
	global_load_lds_dwordx4 v[4:5], off
	v_lshl_add_u64 v[4:5], s[4:5], 0, v[132:133]
	s_add_i32 m0, s59, 0x1e000
	s_cmpk_lt_u32 s1, 0x100
	global_load_lds_dwordx4 v[4:5], off
	s_cselect_b64 s[34:35], -1, 0
	s_ashr_i32 s1, s0, 31
	v_bfe_u32 v5, v15, 4, 2
	s_lshl_b64 s[38:39], s[0:1], 9
	s_or_b32 s1, s28, s0
	v_and_b32_e32 v4, 15, v15
	v_lshlrev_b32_e32 v6, 4, v5
	v_lshlrev_b32_e32 v7, 2, v15
	s_cmp_eq_u32 s1, 0
	v_lshl_or_b32 v6, v4, 6, v6
	v_and_b32_e32 v7, 32, v7
	s_cselect_b64 s[36:37], -1, 0
	s_add_u32 s1, s10, s38
	v_bitop3_b32 v8, v6, s2, v7 bitop3:0xde
	s_addc_u32 s2, s11, s39
	s_lshl_b32 s27, s28, 7
	s_add_u32 s38, s1, s27
	v_lshl_or_b32 v1, s0, 6, v4
	s_waitcnt vmcnt(0)
	v_lshlrev_b32_e32 v138, 3, v5
	v_bitop3_b32 v190, v6, s6, v7 bitop3:0xde
	v_or_b32_e32 v6, v5, v4
	v_cmp_eq_u32_e64 s[6:7], 0, v4
	v_cmp_eq_u32_e64 s[8:9], 0, v5
	s_addc_u32 s39, s2, 0
	v_lshlrev_b32_e32 v4, 5, v5
	v_mov_b32_e32 v5, v3
	v_lshl_add_u64 v[4:5], s[38:39], 0, v[4:5]
	s_mov_b64 s[38:39], 0x59120000
	v_lshl_add_u64 v[140:141], v[4:5], 0, s[38:39]
	v_lshlrev_b32_e32 v4, 16, v17
	v_and_b32_e32 v4, 0xfffe0000, v4
	s_lshl_b32 s1, s28, 2
	v_lshl_add_u32 v4, v16, 13, v4
	v_and_b32_e32 v5, 1, v17
	s_add_u32 s1, s10, s1
	v_lshl_or_b32 v4, v5, 6, v4
	s_addc_u32 s2, s11, 0
	v_lshl_add_u32 v142, v18, 1, v4
	v_lshlrev_b32_e32 v4, 16, v12
	s_add_u32 s1, s1, 0x6f660000
	v_and_b32_e32 v4, 0xfffe0000, v4
	s_waitcnt vmcnt(0)
	v_writelane_b32 v253, s1, 50
	v_lshl_add_u32 v4, v13, 13, v4
	v_and_b32_e32 v5, 1, v12
	v_lshl_or_b32 v4, v5, 6, v4
	v_readlane_b32 s10, v253, 7
	s_mov_b32 s26, 0
	v_cmp_eq_u32_e64 s[4:5], 0, v6
	s_mov_b32 s29, s3
	s_mov_b32 s31, s3
	v_mov_b32_e32 v139, v3
	s_addc_u32 s27, s2, 0
	v_or_b32_e32 v191, s30, v138
	v_mov_b32_e32 v143, v3
	v_lshl_add_u32 v144, v14, 1, v4
	v_mov_b32_e32 v145, v3
	v_add_u32_e32 v196, 0, v8
	v_mov_b32_e32 v192, s65
	v_readlane_b32 s1, v252, 63
	s_mov_b32 s2, s10
	s_barrier
	v_readlane_b32 s11, v253, 8
	s_branch .LBB0_150

; #define PG8_STAGE(bufoff, gbase, voff) do { _Pragma("unroll") for (int _i = 0; _i < 2; ++_i) \
;         __builtin_amdgcn_global_load_lds((const unsigned*)((const char*)(gbase) + (voff)[_i]), (PG8_LAS unsigned*)(lds + (bufoff) + ldsw + _i * 8192), 16, 0, 0); } while (0)
; #define PG8_LDA(dst, b, h) do { _Pragma("unroll") for (int m = 0; m < 4; ++m) _Pragma("unroll") for (int k = 0; k < 2; ++k) dst[m][k] = *(const PG8_LAS bf16x8*)(lds + PG8_SA(b, h) + aoff + m * 2048 + k * 1024); } while (0)
; #define PG8_LDB(dst, b, h) do { _Pragma("unroll") for (int n = 0; n < 2; ++n) _Pragma("unroll") for (int k = 0; k < 2; ++k) dst[n][k] = *(const PG8_LAS bf16x8*)(lds + PG8_SB(b, h) + boff + n * 2048 + k * 1024); } while (0)
; #define PG8_MMA(ai, bj, At, Bt) do { __builtin_amdgcn_s_setprio(1); _Pragma("unroll") for (int m = 0; m < 4; ++m) _Pragma("unroll") for (int n = 0; n < 2; ++n) _Pragma("unroll") for (int k = 0; k < 2; ++k) \
;         acc[ai][bj][m][n] = __builtin_amdgcn_mfma_f32_16x16x32_bf16(Bt[n][k], At[m][k], acc[ai][bj][m][n], 0, 0, 0); __builtin_amdgcn_s_setprio(0); } while (0)
; template <class Epi, class Sched, bool ALIGN_EPI = false, bool SP2 = false>
; __device__ __forceinline__ void gemm_phase(PG8_LAS unsigned char* lds, const Gemm g, const Sched& S, const Epi& E) {
;     ...
;         for (int t = 0; t < nt; t += 2) {
;             const bool last = (t == nt - 2);
;             const char* a1 = cA + (size_t)(t + 1) * kstep;
;             const char* a2 = last ? nA : cA + (size_t)(t + 2) * kstep; const char* b2 = last ? nB : cB + (size_t)(t + 2) * kstep;
;             const char* a3 = a2 + kstep; const char* b3 = b2 + kstep;
;             if (last && has_next) S.a_ready(nxt);
;             if constexpr (Epi::HAS_MID) { if (t != 0 && (t & (Epi::MID_EVERY - 1)) == 0) E.mid(acc, cur, t / Epi::MID_EVERY, wr, wc, fr, fq); }
;             if constexpr (SP2) {
;             PG8_LDB(B0, 0, 0); PG8_LDB(B1, 0, 1); PG8_SCHED; PG8_LDA(At, 0, 0); PG8_STAGE(PG8_SA(1, 1), a1 + hstep, voffA);
;             PG8_WAIT_V(8); PG8_WAIT_L(0); PG8_BAR; PG8_MMA(0, 0, At, B0); PG8_MMA(0, 1, At, B1); PG8_BAR; PG8_SCHED;
;             PG8_LDA(At, 0, 1); PG8_STAGE(PG8_SB(0, 0), b2, voffB); PG8_STAGE(PG8_SB(0, 1), b2 + hstep, voffB); PG8_STAGE(PG8_SA(0, 0), a2, voffA);
;             PG8_WAIT_V(8); PG8_WAIT_L(0); PG8_BAR; PG8_MMA(1, 0, At, B0); PG8_MMA(1, 1, At, B1); PG8_BAR; PG8_SCHED;
.LBB0_153:
	s_add_u32 s46, s12, 0xfff00080
	s_addc_u32 s47, s13, -1
	s_add_i32 s81, 0, 0x10000
	s_cmp_eq_u32 s80, 60
	s_cselect_b32 s49, s41, s47
	s_cselect_b32 s48, s50, s46
	s_cselect_b32 s47, s39, s53
	s_cselect_b32 s46, s51, s52
	s_add_i32 s84, 0, 0x14000
	v_add_u32_e32 v158, s81, v190
	v_add_u32_e32 v174, s84, v190
	s_waitcnt lgkmcnt(0)
	ds_read_b128 v[146:149], v158
	ds_read_b128 v[150:153], v158 offset:1024
	ds_read_b128 v[154:157], v158 offset:2048
	ds_read_b128 v[158:161], v158 offset:3072
	ds_read_b128 v[162:165], v174
	ds_read_b128 v[166:169], v174 offset:1024
	ds_read_b128 v[170:173], v174 offset:2048
	ds_read_b128 v[174:177], v174 offset:3072
	v_lshl_add_u64 v[194:195], s[12:13], 0, v[142:143]
	s_add_i32 m0, s59, 0xc000
	ds_read_b128 v[178:181], v196
	ds_read_b128 v[182:185], v196 offset:1024
	ds_read_b128 v[186:189], v196 offset:2048
	ds_read_b128 v[198:201], v196 offset:3072
	ds_read_b128 v[202:205], v196 offset:4096
	ds_read_b128 v[206:209], v196 offset:5120
	ds_read_b128 v[210:213], v196 offset:6144
	ds_read_b128 v[214:217], v196 offset:7168
	global_load_lds_dwordx4 v[194:195], off
	v_lshl_add_u64 v[194:195], s[12:13], 0, v[144:145]
	s_add_i32 m0, s59, 0xe000
	s_nop 0
	global_load_lds_dwordx4 v[194:195], off
	s_cmp_eq_u32 s80, -2
	s_cbranch_scc1 .Lp1_w0_skip
	s_waitcnt vmcnt(8)
.Lp1_w0_skip:
	s_waitcnt lgkmcnt(0)
	s_barrier
	s_setprio 1
	s_waitcnt lgkmcnt(0)
	v_mfma_f32_16x16x32_bf16 v[128:131], v[146:149], v[178:181], v[128:131]
	v_mfma_f32_16x16x32_bf16 v[124:127], v[154:157], v[178:181], v[124:127]
	v_mfma_f32_16x16x32_bf16 v[112:115], v[146:149], v[186:189], v[112:115]
	v_mfma_f32_16x16x32_bf16 v[108:111], v[154:157], v[186:189], v[108:111]
	v_mfma_f32_16x16x32_bf16 v[96:99], v[146:149], v[202:205], v[96:99]
	v_mfma_f32_16x16x32_bf16 v[92:95], v[154:157], v[202:205], v[92:95]
	v_mfma_f32_16x16x32_bf16 v[80:83], v[146:149], v[210:213], v[80:83]
	v_mfma_f32_16x16x32_bf16 v[76:79], v[154:157], v[210:213], v[76:79]
	v_mfma_f32_16x16x32_bf16 v[128:131], v[150:153], v[182:185], v[128:131]
	v_mfma_f32_16x16x32_bf16 v[124:127], v[158:161], v[182:185], v[124:127]
	v_mfma_f32_16x16x32_bf16 v[112:115], v[150:153], v[198:201], v[112:115]
	v_mfma_f32_16x16x32_bf16 v[108:111], v[158:161], v[198:201], v[108:111]
	v_mfma_f32_16x16x32_bf16 v[96:99], v[150:153], v[206:209], v[96:99]
	v_mfma_f32_16x16x32_bf16 v[92:95], v[158:161], v[206:209], v[92:95]
	v_mfma_f32_16x16x32_bf16 v[80:83], v[150:153], v[214:217], v[80:83]
	v_mfma_f32_16x16x32_bf16 v[76:79], v[158:161], v[214:217], v[76:79]
	s_setprio 0
	s_setprio 1
	v_mfma_f32_16x16x32_bf16 v[120:123], v[162:165], v[178:181], v[120:123]
	v_mfma_f32_16x16x32_bf16 v[116:119], v[170:173], v[178:181], v[116:119]
	v_mfma_f32_16x16x32_bf16 v[104:107], v[162:165], v[186:189], v[104:107]
	v_mfma_f32_16x16x32_bf16 v[100:103], v[170:173], v[186:189], v[100:103]
	v_mfma_f32_16x16x32_bf16 v[88:91], v[162:165], v[202:205], v[88:91]
	v_mfma_f32_16x16x32_bf16 v[84:87], v[170:173], v[202:205], v[84:87]
	v_mfma_f32_16x16x32_bf16 v[72:75], v[162:165], v[210:213], v[72:75]
	v_mfma_f32_16x16x32_bf16 v[68:71], v[170:173], v[210:213], v[68:71]
	v_mfma_f32_16x16x32_bf16 v[120:123], v[166:169], v[182:185], v[120:123]
	v_mfma_f32_16x16x32_bf16 v[116:119], v[174:177], v[182:185], v[116:119]
	v_mfma_f32_16x16x32_bf16 v[104:107], v[166:169], v[198:201], v[104:107]
	v_mfma_f32_16x16x32_bf16 v[100:103], v[174:177], v[198:201], v[100:103]
	v_mfma_f32_16x16x32_bf16 v[88:91], v[166:169], v[206:209], v[88:91]
	v_mfma_f32_16x16x32_bf16 v[84:87], v[174:177], v[206:209], v[84:87]
	v_mfma_f32_16x16x32_bf16 v[72:75], v[166:169], v[214:217], v[72:75]
	v_mfma_f32_16x16x32_bf16 v[68:71], v[174:177], v[214:217], v[68:71]
	s_setprio 0
	s_barrier
	s_add_i32 s81, s81, s58
	v_lshl_add_u64 v[194:195], s[46:47], 0, v[2:3]
	s_mov_b32 m0, s81
	ds_read_b128 v[178:181], v196 offset:16384
	ds_read_b128 v[182:185], v196 offset:17408
	ds_read_b128 v[186:189], v196 offset:18432
	ds_read_b128 v[198:201], v196 offset:19456
	ds_read_b128 v[202:205], v196 offset:20480
	ds_read_b128 v[206:209], v196 offset:21504
	ds_read_b128 v[210:213], v196 offset:22528
	ds_read_b128 v[214:217], v196 offset:23552
	global_load_lds_dwordx4 v[194:195], off
	s_add_i32 m0, s81, 0x2000
	s_add_u32 s82, s46, 0x100000
	v_lshl_add_u64 v[222:223], s[46:47], 0, v[132:133]
	s_addc_u32 s83, s47, 0
	s_add_i32 s81, s84, s58
	global_load_lds_dwordx4 v[222:223], off
	v_lshl_add_u64 v[232:233], s[82:83], 0, v[2:3]
	s_mov_b32 m0, s81
	v_lshl_add_u64 v[234:235], s[48:49], 0, v[134:135]
	global_load_lds_dwordx4 v[232:233], off
	v_lshl_add_u64 v[232:233], s[82:83], 0, v[132:133]
	s_add_i32 m0, s81, 0x2000
	s_nop 0
	global_load_lds_dwordx4 v[232:233], off
	v_lshl_add_u64 v[232:233], s[48:49], 0, v[136:137]
	s_mov_b32 m0, s59
	s_nop 0
	global_load_lds_dwordx4 v[232:233], off
	s_mov_b32 m0, s60
	s_nop 0
	global_load_lds_dwordx4 v[234:235], off
	s_cmp_eq_u32 s80, -2
	s_cbranch_scc1 .Lp1_w1_skip
	s_waitcnt vmcnt(8)
; #define PG8_STAGE(bufoff, gbase, voff) do { _Pragma("unroll") for (int _i = 0; _i < 2; ++_i) \
;         __builtin_amdgcn_global_load_lds((const unsigned*)((const char*)(gbase) + (voff)[_i]), (PG8_LAS unsigned*)(lds + (bufoff) + ldsw + _i * 8192), 16, 0, 0); } while (0)
; #define PG8_LDA(dst, b, h) do { _Pragma("unroll") for (int m = 0; m < 4; ++m) _Pragma("unroll") for (int k = 0; k < 2; ++k) dst[m][k] = *(const PG8_LAS bf16x8*)(lds + PG8_SA(b, h) + aoff + m * 2048 + k * 1024); } while (0)
; #define PG8_LDB(dst, b, h) do { _Pragma("unroll") for (int n = 0; n < 2; ++n) _Pragma("unroll") for (int k = 0; k < 2; ++k) dst[n][k] = *(const PG8_LAS bf16x8*)(lds + PG8_SB(b, h) + boff + n * 2048 + k * 1024); } while (0)
; #define PG8_MMA(ai, bj, At, Bt) do { __builtin_amdgcn_s_setprio(1); _Pragma("unroll") for (int m = 0; m < 4; ++m) _Pragma("unroll") for (int n = 0; n < 2; ++n) _Pragma("unroll") for (int k = 0; k < 2; ++k) \
;         acc[ai][bj][m][n] = __builtin_amdgcn_mfma_f32_16x16x32_bf16(Bt[n][k], At[m][k], acc[ai][bj][m][n], 0, 0, 0); __builtin_amdgcn_s_setprio(0); } while (0)
; #define PG8_WAIT_V(n) asm volatile("s_waitcnt vmcnt(" #n ")" ::: "memory")
; #define PG8_WAIT_L(n) asm volatile("s_waitcnt lgkmcnt(" #n ")" ::: "memory")
; #define PG8_BAR __builtin_amdgcn_s_barrier()
; #define PG8_SCHED __builtin_amdgcn_sched_barrier(0)
; template <class Epi, class Sched, bool ALIGN_EPI = false, bool SP2 = false>
; __device__ __forceinline__ void gemm_phase(PG8_LAS unsigned char* lds, const Gemm g, const Sched& S, const Epi& E) {
;     ...
;             PG8_WAIT_V(8); PG8_WAIT_L(0); PG8_BAR; PG8_MMA(1, 0, At, B0); PG8_MMA(1, 1, At, B1); PG8_BAR; PG8_SCHED;
;             PG8_LDB(B0, 1, 0); PG8_LDB(B1, 1, 1); PG8_SCHED; PG8_LDA(At, 1, 0); PG8_STAGE(PG8_SA(0, 1), a2 + hstep, voffA);
;             PG8_WAIT_V(8); PG8_WAIT_L(0); PG8_BAR; PG8_MMA(0, 0, At, B0); PG8_MMA(0, 1, At, B1); PG8_BAR; PG8_SCHED;
.Lp1_w1_skip:
	s_waitcnt lgkmcnt(0)
	s_barrier
	s_setprio 1
	s_waitcnt lgkmcnt(0)
	v_mfma_f32_16x16x32_bf16 v[64:67], v[146:149], v[178:181], v[64:67]
	v_mfma_f32_16x16x32_bf16 v[60:63], v[154:157], v[178:181], v[60:63]
	v_mfma_f32_16x16x32_bf16 v[48:51], v[146:149], v[186:189], v[48:51]
	v_mfma_f32_16x16x32_bf16 v[44:47], v[154:157], v[186:189], v[44:47]
	v_mfma_f32_16x16x32_bf16 v[32:35], v[146:149], v[202:205], v[32:35]
	v_mfma_f32_16x16x32_bf16 v[28:31], v[154:157], v[202:205], v[28:31]
	v_mfma_f32_16x16x32_bf16 v[16:19], v[146:149], v[210:213], v[16:19]
	v_mfma_f32_16x16x32_bf16 v[12:15], v[154:157], v[210:213], v[12:15]
	v_mfma_f32_16x16x32_bf16 v[64:67], v[150:153], v[182:185], v[64:67]
	v_mfma_f32_16x16x32_bf16 v[60:63], v[158:161], v[182:185], v[60:63]
	v_mfma_f32_16x16x32_bf16 v[48:51], v[150:153], v[198:201], v[48:51]
	v_mfma_f32_16x16x32_bf16 v[44:47], v[158:161], v[198:201], v[44:47]
	v_mfma_f32_16x16x32_bf16 v[32:35], v[150:153], v[206:209], v[32:35]
	v_mfma_f32_16x16x32_bf16 v[28:31], v[158:161], v[206:209], v[28:31]
	v_mfma_f32_16x16x32_bf16 v[16:19], v[150:153], v[214:217], v[16:19]
	v_mfma_f32_16x16x32_bf16 v[12:15], v[158:161], v[214:217], v[12:15]
	s_setprio 0
	s_setprio 1
	v_mfma_f32_16x16x32_bf16 v[56:59], v[162:165], v[178:181], v[56:59]
	v_mfma_f32_16x16x32_bf16 v[52:55], v[170:173], v[178:181], v[52:55]
	v_mfma_f32_16x16x32_bf16 v[40:43], v[162:165], v[186:189], v[40:43]
	v_mfma_f32_16x16x32_bf16 v[36:39], v[170:173], v[186:189], v[36:39]
	v_mfma_f32_16x16x32_bf16 v[24:27], v[162:165], v[202:205], v[24:27]
	v_mfma_f32_16x16x32_bf16 v[20:23], v[170:173], v[202:205], v[20:23]
	v_mfma_f32_16x16x32_bf16 v[8:11], v[162:165], v[210:213], v[8:11]
	v_mfma_f32_16x16x32_bf16 v[4:7], v[170:173], v[210:213], v[4:7]
	v_mfma_f32_16x16x32_bf16 v[56:59], v[166:169], v[182:185], v[56:59]
	v_mfma_f32_16x16x32_bf16 v[52:55], v[174:177], v[182:185], v[52:55]
	v_mfma_f32_16x16x32_bf16 v[40:43], v[166:169], v[198:201], v[40:43]
	v_mfma_f32_16x16x32_bf16 v[36:39], v[174:177], v[198:201], v[36:39]
	v_mfma_f32_16x16x32_bf16 v[24:27], v[166:169], v[206:209], v[24:27]
	v_mfma_f32_16x16x32_bf16 v[20:23], v[174:177], v[206:209], v[20:23]
	v_mfma_f32_16x16x32_bf16 v[8:11], v[166:169], v[214:217], v[8:11]
	v_mfma_f32_16x16x32_bf16 v[4:7], v[174:177], v[214:217], v[4:7]
	s_setprio 0
	s_barrier
	s_add_i32 s81, 0, 0x18000
	s_add_i32 s82, 0, 0x1c000
	v_add_u32_e32 v158, s81, v190
	v_add_u32_e32 v174, s82, v190
	ds_read_b128 v[146:149], v158
	ds_read_b128 v[150:153], v158 offset:1024
	ds_read_b128 v[154:157], v158 offset:2048
	ds_read_b128 v[158:161], v158 offset:3072
	ds_read_b128 v[162:165], v174
	ds_read_b128 v[166:169], v174 offset:1024
	ds_read_b128 v[170:173], v174 offset:2048
	ds_read_b128 v[174:177], v174 offset:3072
	s_add_u32 s48, s48, 0x100000
	s_addc_u32 s49, s49, 0
	s_mov_b32 m0, s61
	v_lshl_add_u64 v[236:237], s[48:49], 0, v[136:137]
	ds_read_b128 v[178:181], v196 offset:32768
	ds_read_b128 v[182:185], v196 offset:33792
	ds_read_b128 v[186:189], v196 offset:34816
	ds_read_b128 v[198:201], v196 offset:35840
	ds_read_b128 v[202:205], v196 offset:36864
	ds_read_b128 v[206:209], v196 offset:37888
	ds_read_b128 v[210:213], v196 offset:38912
	ds_read_b128 v[214:217], v196 offset:39936
	global_load_lds_dwordx4 v[236:237], off
	v_lshl_add_u64 v[236:237], s[48:49], 0, v[134:135]
	s_mov_b32 m0, s62
	s_nop 0
	global_load_lds_dwordx4 v[236:237], off
	s_waitcnt vmcnt(8)
	s_waitcnt lgkmcnt(0)
	s_barrier
	s_setprio 1
	s_waitcnt lgkmcnt(0)
	v_mfma_f32_16x16x32_bf16 v[128:131], v[146:149], v[178:181], v[128:131]
	v_mfma_f32_16x16x32_bf16 v[124:127], v[154:157], v[178:181], v[124:127]
	v_mfma_f32_16x16x32_bf16 v[112:115], v[146:149], v[186:189], v[112:115]
	v_mfma_f32_16x16x32_bf16 v[108:111], v[154:157], v[186:189], v[108:111]
	v_mfma_f32_16x16x32_bf16 v[96:99], v[146:149], v[202:205], v[96:99]
	v_mfma_f32_16x16x32_bf16 v[92:95], v[154:157], v[202:205], v[92:95]
	v_mfma_f32_16x16x32_bf16 v[80:83], v[146:149], v[210:213], v[80:83]
	v_mfma_f32_16x16x32_bf16 v[76:79], v[154:157], v[210:213], v[76:79]
	v_mfma_f32_16x16x32_bf16 v[128:131], v[150:153], v[182:185], v[128:131]
	v_mfma_f32_16x16x32_bf16 v[124:127], v[158:161], v[182:185], v[124:127]
	v_mfma_f32_16x16x32_bf16 v[112:115], v[150:153], v[198:201], v[112:115]
	v_mfma_f32_16x16x32_bf16 v[108:111], v[158:161], v[198:201], v[108:111]
	v_mfma_f32_16x16x32_bf16 v[96:99], v[150:153], v[206:209], v[96:99]
	v_mfma_f32_16x16x32_bf16 v[92:95], v[158:161], v[206:209], v[92:95]
	v_mfma_f32_16x16x32_bf16 v[80:83], v[150:153], v[214:217], v[80:83]
	v_mfma_f32_16x16x32_bf16 v[76:79], v[158:161], v[214:217], v[76:79]
	s_setprio 0
	s_setprio 1
	v_mfma_f32_16x16x32_bf16 v[120:123], v[162:165], v[178:181], v[120:123]
	v_mfma_f32_16x16x32_bf16 v[116:119], v[170:173], v[178:181], v[116:119]
	v_mfma_f32_16x16x32_bf16 v[104:107], v[162:165], v[186:189], v[104:107]
	v_mfma_f32_16x16x32_bf16 v[100:103], v[170:173], v[186:189], v[100:103]
	v_mfma_f32_16x16x32_bf16 v[88:91], v[162:165], v[202:205], v[88:91]
	v_mfma_f32_16x16x32_bf16 v[84:87], v[170:173], v[202:205], v[84:87]
	v_mfma_f32_16x16x32_bf16 v[72:75], v[162:165], v[210:213], v[72:75]
	v_mfma_f32_16x16x32_bf16 v[68:71], v[170:173], v[210:213], v[68:71]
	v_mfma_f32_16x16x32_bf16 v[120:123], v[166:169], v[182:185], v[120:123]
	v_mfma_f32_16x16x32_bf16 v[116:119], v[174:177], v[182:185], v[116:119]
	v_mfma_f32_16x16x32_bf16 v[104:107], v[166:169], v[198:201], v[104:107]
	v_mfma_f32_16x16x32_bf16 v[100:103], v[174:177], v[198:201], v[100:103]
	v_mfma_f32_16x16x32_bf16 v[88:91], v[166:169], v[206:209], v[88:91]
	v_mfma_f32_16x16x32_bf16 v[84:87], v[174:177], v[206:209], v[84:87]
	v_mfma_f32_16x16x32_bf16 v[72:75], v[166:169], v[214:217], v[72:75]
	v_mfma_f32_16x16x32_bf16 v[68:71], v[174:177], v[214:217], v[68:71]
	s_setprio 0
	s_barrier
; #define PG8_STAGE(bufoff, gbase, voff) do { _Pragma("unroll") for (int _i = 0; _i < 2; ++_i) \
;         __builtin_amdgcn_global_load_lds((const unsigned*)((const char*)(gbase) + (voff)[_i]), (PG8_LAS unsigned*)(lds + (bufoff) + ldsw + _i * 8192), 16, 0, 0); } while (0)
; #define PG8_LDA(dst, b, h) do { _Pragma("unroll") for (int m = 0; m < 4; ++m) _Pragma("unroll") for (int k = 0; k < 2; ++k) dst[m][k] = *(const PG8_LAS bf16x8*)(lds + PG8_SA(b, h) + aoff + m * 2048 + k * 1024); } while (0)
; #define PG8_MMA(ai, bj, At, Bt) do { __builtin_amdgcn_s_setprio(1); _Pragma("unroll") for (int m = 0; m < 4; ++m) _Pragma("unroll") for (int n = 0; n < 2; ++n) _Pragma("unroll") for (int k = 0; k < 2; ++k) \
;         acc[ai][bj][m][n] = __builtin_amdgcn_mfma_f32_16x16x32_bf16(Bt[n][k], At[m][k], acc[ai][bj][m][n], 0, 0, 0); __builtin_amdgcn_s_setprio(0); } while (0)
; #define PG8_WAIT_V(n) asm volatile("s_waitcnt vmcnt(" #n ")" ::: "memory")
; #define PG8_WAIT_L(n) asm volatile("s_waitcnt lgkmcnt(" #n ")" ::: "memory")
; #define PG8_BAR __builtin_amdgcn_s_barrier()
; #define PG8_SCHED __builtin_amdgcn_sched_barrier(0)
; template <class Epi, class Sched, bool ALIGN_EPI = false, bool SP2 = false>
; __device__ __forceinline__ void gemm_phase(PG8_LAS unsigned char* lds, const Gemm g, const Sched& S, const Epi& E) {
;     ...
;         for (int t = 0; t < nt; t += 2) {
;     ...
;             PG8_LDA(At, 1, 1); PG8_STAGE(PG8_SB(1, 0), b3, voffB); PG8_STAGE(PG8_SB(1, 1), b3 + hstep, voffB); PG8_STAGE(PG8_SA(1, 0), a3, voffA);
;             PG8_WAIT_V(8); PG8_WAIT_L(0); PG8_BAR; PG8_MMA(1, 0, At, B0); PG8_MMA(1, 1, At, B1); PG8_BAR; PG8_SCHED;
	s_add_i32 s48, s81, s58
	v_lshl_add_u64 v[194:195], v[194:195], 0, s[78:79]
	s_mov_b32 m0, s48
	ds_read_b128 v[178:181], v196 offset:49152
	ds_read_b128 v[182:185], v196 offset:50176
	ds_read_b128 v[186:189], v196 offset:51200
	ds_read_b128 v[198:201], v196 offset:52224
	ds_read_b128 v[202:205], v196 offset:53248
	ds_read_b128 v[206:209], v196 offset:54272
	ds_read_b128 v[210:213], v196 offset:55296
	ds_read_b128 v[214:217], v196 offset:56320
	global_load_lds_dwordx4 v[194:195], off
	s_add_i32 m0, s48, 0x2000
	s_add_u32 s46, s46, 0x100080
	v_lshl_add_u64 v[194:195], v[222:223], 0, s[78:79]
	s_addc_u32 s47, s47, 0
	s_add_i32 s48, s82, s58
	global_load_lds_dwordx4 v[194:195], off
	v_lshl_add_u64 v[194:195], s[46:47], 0, v[2:3]
	s_mov_b32 m0, s48
	s_nop 0
	global_load_lds_dwordx4 v[194:195], off
	v_lshl_add_u64 v[194:195], s[46:47], 0, v[132:133]
	s_add_i32 m0, s48, 0x2000
	s_nop 0
	global_load_lds_dwordx4 v[194:195], off
	v_lshl_add_u64 v[194:195], v[232:233], 0, s[78:79]
	s_mov_b32 m0, s66
	s_nop 0
	global_load_lds_dwordx4 v[194:195], off
	v_lshl_add_u64 v[194:195], v[234:235], 0, s[78:79]
	s_mov_b32 m0, s67
	s_nop 0
	global_load_lds_dwordx4 v[194:195], off
	s_waitcnt vmcnt(8)
	s_waitcnt lgkmcnt(0)
	s_barrier
	s_setprio 1
	s_waitcnt lgkmcnt(0)
	v_mfma_f32_16x16x32_bf16 v[64:67], v[146:149], v[178:181], v[64:67]
	v_mfma_f32_16x16x32_bf16 v[60:63], v[154:157], v[178:181], v[60:63]
	v_mfma_f32_16x16x32_bf16 v[48:51], v[146:149], v[186:189], v[48:51]
	v_mfma_f32_16x16x32_bf16 v[44:47], v[154:157], v[186:189], v[44:47]
	v_mfma_f32_16x16x32_bf16 v[32:35], v[146:149], v[202:205], v[32:35]
	v_mfma_f32_16x16x32_bf16 v[28:31], v[154:157], v[202:205], v[28:31]
	v_mfma_f32_16x16x32_bf16 v[16:19], v[146:149], v[210:213], v[16:19]
	v_mfma_f32_16x16x32_bf16 v[12:15], v[154:157], v[210:213], v[12:15]
	v_mfma_f32_16x16x32_bf16 v[64:67], v[150:153], v[182:185], v[64:67]
	v_mfma_f32_16x16x32_bf16 v[60:63], v[158:161], v[182:185], v[60:63]
	v_mfma_f32_16x16x32_bf16 v[48:51], v[150:153], v[198:201], v[48:51]
	v_mfma_f32_16x16x32_bf16 v[44:47], v[158:161], v[198:201], v[44:47]
	v_mfma_f32_16x16x32_bf16 v[32:35], v[150:153], v[206:209], v[32:35]
	v_mfma_f32_16x16x32_bf16 v[28:31], v[158:161], v[206:209], v[28:31]
	v_mfma_f32_16x16x32_bf16 v[16:19], v[150:153], v[214:217], v[16:19]
	v_mfma_f32_16x16x32_bf16 v[12:15], v[158:161], v[214:217], v[12:15]
	s_setprio 0
	s_setprio 1
	v_mfma_f32_16x16x32_bf16 v[56:59], v[162:165], v[178:181], v[56:59]
	v_mfma_f32_16x16x32_bf16 v[52:55], v[170:173], v[178:181], v[52:55]
	v_mfma_f32_16x16x32_bf16 v[40:43], v[162:165], v[186:189], v[40:43]
	v_mfma_f32_16x16x32_bf16 v[36:39], v[170:173], v[186:189], v[36:39]
	v_mfma_f32_16x16x32_bf16 v[24:27], v[162:165], v[202:205], v[24:27]
	v_mfma_f32_16x16x32_bf16 v[20:23], v[170:173], v[202:205], v[20:23]
	v_mfma_f32_16x16x32_bf16 v[8:11], v[162:165], v[210:213], v[8:11]
	v_mfma_f32_16x16x32_bf16 v[4:7], v[170:173], v[210:213], v[4:7]
	v_mfma_f32_16x16x32_bf16 v[56:59], v[166:169], v[182:185], v[56:59]
	v_mfma_f32_16x16x32_bf16 v[52:55], v[174:177], v[182:185], v[52:55]
	v_mfma_f32_16x16x32_bf16 v[40:43], v[166:169], v[198:201], v[40:43]
	v_mfma_f32_16x16x32_bf16 v[36:39], v[174:177], v[198:201], v[36:39]
	v_mfma_f32_16x16x32_bf16 v[24:27], v[166:169], v[206:209], v[24:27]
	v_mfma_f32_16x16x32_bf16 v[20:23], v[174:177], v[206:209], v[20:23]
	v_mfma_f32_16x16x32_bf16 v[8:11], v[166:169], v[214:217], v[8:11]
	v_mfma_f32_16x16x32_bf16 v[4:7], v[174:177], v[214:217], v[4:7]
	s_setprio 0
	s_barrier
	s_add_i32 s80, s80, 2
	s_add_u32 s12, s12, 0x100
	s_addc_u32 s13, s13, 0
	s_add_u32 s52, s52, 0x100
	s_addc_u32 s53, s53, 0
	s_cmp_gt_u32 s80, 61
	s_cbranch_scc0 .LBB0_153
	s_and_b64 vcc, exec, s[34:35]
	s_cbranch_vccnz .LBB0_164
	s_ashr_i32 s39, s1, 2
	s_cmp_lt_i32 s39, 13
	s_mov_b64 s[12:13], -1
	s_cbranch_scc1 .LBB0_165
